# speedup vs baseline: 1.0329x; 1.0012x over previous
.LBB8_5:
	s_ashr_i32 s28, s7, 3
	v_lshlrev_b32_e32 v2, 9, v178
	s_movk_i32 s7, 0x1e00
	v_and_or_b32 v2, v2, s7, v177
	v_lshlrev_b32_e32 v183, 1, v2
	v_mul_lo_u32 v2, s6, v182
	v_add_lshl_u32 v162, v2, v177, 1
	v_lshlrev_b32_e32 v2, 6, v181
	s_movk_i32 s7, 0xc00
	s_lshl_b32 s43, s26, 3
	v_and_or_b32 v184, v2, s7, v176
	v_mul_lo_u32 v2, s6, v180
	s_abs_i32 s44, s43
	v_add_lshl_u32 v164, v2, v177, 1
	v_cvt_f32_u32_e32 v2, s44
	s_sub_i32 s29, 0, s44
	s_add_i32 s27, s27, s28
	s_ashr_i32 s28, s27, 31
	v_rcp_iflag_f32_e32 v2, v2
	s_bfe_i32 s46, s26, 0x1001c
	s_xor_b32 s26, s28, s46
	s_abs_i32 s28, s27
	v_mul_f32_e32 v2, 0x4f7ffffe, v2
	v_cvt_u32_f32_e32 v2, v2
	s_lshr_b32 s36, s19, 6
	s_ashr_i32 s7, s6, 31
	s_lshr_b32 s37, s19, 8
	v_readfirstlane_b32 s47, v2
	s_mul_i32 s29, s29, s47
	s_mul_hi_u32 s29, s47, s29
	s_add_i32 s47, s47, s29
	s_mul_hi_u32 s29, s28, s47
	s_mul_i32 s30, s29, s44
	s_sub_i32 s28, s28, s30
	s_lshl_b64 s[22:23], s[6:7], 8
	s_lshl_b64 s[24:25], s[6:7], 9
	s_lshl_b32 s45, s36, 10
	s_add_i32 s30, s29, 1
	s_sub_i32 s31, s28, s44
	s_cmp_ge_u32 s28, s44
	s_cselect_b32 s29, s30, s29
	s_cselect_b32 s28, s31, s28
	s_add_i32 s30, s29, 1
	s_cmp_ge_u32 s28, s44
	s_cselect_b32 s28, s30, s29
	s_xor_b32 s28, s28, s26
	s_sub_i32 s26, s28, s26
	s_lshl_b32 s28, s26, 3
	s_sub_i32 s29, s33, s28
	s_min_i32 s29, s29, 8
	s_abs_i32 s30, s29
	v_cvt_f32_u32_e32 v2, s30
	s_sub_i32 s34, 0, s30
	s_mul_i32 s26, s26, s43
	v_lshlrev_b32_e32 v3, 6, v179
	v_rcp_iflag_f32_e32 v2, v2
	s_movk_i32 s31, 0x1c00
	s_sub_i32 s26, s27, s26
	v_and_or_b32 v185, v3, s31, v176
	v_mul_f32_e32 v2, 0x4f7ffffe, v2
	v_cvt_u32_f32_e32 v2, v2
	s_abs_i32 s31, s26
	s_xor_b32 s27, s26, s29
	s_ashr_i32 s27, s27, 31
	v_readfirstlane_b32 s35, v2
	s_mul_i32 s34, s34, s35
	s_mul_hi_u32 s34, s35, s34
	s_add_i32 s35, s35, s34
	s_mul_hi_u32 s34, s31, s35
	s_mul_i32 s35, s34, s30
	s_sub_i32 s31, s31, s35
	s_add_i32 s35, s34, 1
	s_sub_i32 s48, s31, s30
	s_cmp_ge_u32 s31, s30
	s_cselect_b32 s34, s35, s34
	s_cselect_b32 s31, s48, s31
	s_add_i32 s35, s34, 1
	s_cmp_ge_u32 s31, s30
	s_cselect_b32 s30, s35, s34
	s_xor_b32 s30, s30, s27
	s_sub_i32 s58, s30, s27
	s_mul_i32 s27, s58, s29
	s_sub_i32 s26, s26, s27
	s_add_i32 s57, s26, s28
	s_ashr_i32 s26, s58, 31
	s_mul_i32 s26, s24, s26
	s_mul_hi_u32 s27, s24, s58
	s_add_i32 s28, s27, s26
	s_lshr_b64 s[26:27], s[6:7], 23
	s_mul_i32 s26, s26, s58
	s_add_i32 s28, s28, s26
	s_mul_i32 s26, s24, s58
	s_waitcnt lgkmcnt(0)
	s_add_u32 s34, s20, s26
	s_addc_u32 s35, s21, s28
	s_lshl_b32 s26, s57, 13
	s_ashr_i32 s27, s26, 31
	s_lshl_b64 s[26:27], s[26:27], 1
	s_add_u32 s28, s8, s26
	s_addc_u32 s29, s9, s27
	s_lshl_b32 s26, s57, 14
	s_ashr_i32 s27, s26, 31
	s_lshl_b64 s[26:27], s[26:27], 1
	s_add_u32 s30, s10, s26
	s_nop 4
	global_load_dwordx4 v[6:9], v184, s[28:29]
	s_addc_u32 s31, s11, s27
	global_load_dwordx4 v[10:13], v185, s[28:29]
	s_add_i32 s52, s45, 0
	global_load_dwordx4 v[14:17], v183, s[30:31]
	s_add_i32 m0, s52, 0x10000
	v_mov_b32_e32 v163, 0
	global_load_lds_dwordx4 v162, s[34:35]
	s_add_i32 m0, s52, 0x12000
	v_mov_b32_e32 v2, v163
	global_load_lds_dwordx4 v164, s[34:35]
	v_mov_b32_e32 v3, v163
	v_mov_b32_e32 v4, v163
	v_mov_b32_e32 v5, v163
	v_mov_b64_e32 v[26:27], 0
	v_mov_b64_e32 v[28:29], 0
	v_mov_b64_e32 v[30:31], 0
	v_mov_b64_e32 v[32:33], 0
	v_mov_b64_e32 v[34:35], 0
	v_mov_b64_e32 v[36:37], 0
	v_mov_b64_e32 v[38:39], 0
	v_mov_b64_e32 v[40:41], 0
	v_mov_b64_e32 v[42:43], 0
	v_mov_b64_e32 v[44:45], 0
	v_mov_b64_e32 v[46:47], 0
	v_mov_b64_e32 v[48:49], 0
	v_mov_b64_e32 v[50:51], 0
	v_mov_b64_e32 v[52:53], 0
	v_mov_b64_e32 v[54:55], 0
	v_mov_b64_e32 v[56:57], 0
	v_mov_b64_e32 v[58:59], 0
	v_mov_b64_e32 v[60:61], 0
	v_mov_b64_e32 v[62:63], 0
	v_mov_b64_e32 v[64:65], 0
	v_mov_b64_e32 v[66:67], 0
	v_mov_b64_e32 v[68:69], 0
	v_mov_b64_e32 v[70:71], 0
	v_mov_b64_e32 v[72:73], 0
	v_mov_b64_e32 v[74:75], 0
	v_mov_b64_e32 v[76:77], 0
	v_mov_b64_e32 v[78:79], 0
	v_mov_b64_e32 v[80:81], 0
	v_mov_b64_e32 v[82:83], 0
	v_mov_b64_e32 v[84:85], 0
	v_mov_b64_e32 v[86:87], 0
	v_mov_b64_e32 v[88:89], 0
	v_mov_b64_e32 v[90:91], 0
	v_mov_b64_e32 v[92:93], 0
	v_mov_b64_e32 v[94:95], 0
	v_mov_b64_e32 v[96:97], 0
	v_mov_b64_e32 v[98:99], 0
	v_mov_b64_e32 v[100:101], 0
	v_mov_b64_e32 v[102:103], 0
	v_mov_b64_e32 v[104:105], 0
	v_mov_b64_e32 v[106:107], 0
	v_mov_b64_e32 v[108:109], 0
	v_mov_b64_e32 v[110:111], 0
	v_mov_b64_e32 v[112:113], 0
	v_mov_b64_e32 v[114:115], 0
	v_mov_b64_e32 v[116:117], 0
	v_mov_b64_e32 v[118:119], 0
	v_mov_b64_e32 v[120:121], 0
	v_mov_b64_e32 v[122:123], 0
	v_mov_b64_e32 v[124:125], 0
	v_mov_b64_e32 v[126:127], 0
	v_mov_b64_e32 v[128:129], 0
	v_mov_b64_e32 v[130:131], 0
	v_mov_b64_e32 v[132:133], 0
	v_mov_b64_e32 v[134:135], 0
	v_mov_b64_e32 v[136:137], 0
	v_mov_b64_e32 v[138:139], 0
	v_mov_b64_e32 v[140:141], 0
	v_mov_b64_e32 v[142:143], 0
	v_mov_b64_e32 v[144:145], 0
	s_waitcnt vmcnt(2)
	s_add_u32 s26, s28, 0x2000
	v_pk_add_f16 v6, v6, v14
	v_pk_add_f16 v7, v7, v15
	v_pk_add_f16 v8, v8, v16
	v_pk_add_f16 v9, v9, v17
	v_pk_max_f16 v8, v8, 0
	v_pk_max_f16 v9, v9, 0
	v_pk_max_f16 v7, v7, 0
	v_pk_max_f16 v6, v6, 0
	v_pk_add_f16 v10, v10, v14
	v_pk_add_f16 v11, v11, v15
	v_pk_add_f16 v12, v12, v16
	v_pk_add_f16 v13, v13, v17
	v_add_u32_e32 v186, 0, v1
	s_addc_u32 s27, s29, 0
	v_pk_max_f16 v13, v13, 0
	v_pk_max_f16 v12, v12, 0
	v_pk_max_f16 v11, v11, 0
	v_pk_max_f16 v10, v10, 0
	ds_write_b128 v186, v[6:9]
	ds_write_b128 v186, v[10:13] offset:8192
	s_add_u32 s48, s30, 0x4000
	s_addc_u32 s49, s31, 0
	s_nop 4
	global_load_dwordx4 v[6:9], v184, s[26:27]
	global_load_dwordx4 v[10:13], v185, s[26:27]
	s_add_u32 s26, s34, s22
	global_load_dwordx4 v[14:17], v183, s[48:49]
	s_addc_u32 s27, s35, s23
	s_add_i32 m0, s52, 0x14000
	v_mov_b32_e32 v165, v163
	global_load_lds_dwordx4 v162, s[26:27]
	s_add_i32 m0, s52, 0x16000
	s_add_u32 s48, s28, 0x80
	global_load_lds_dwordx4 v164, s[26:27]
	s_waitcnt vmcnt(2)
	s_addc_u32 s49, s29, 0
	v_pk_add_f16 v6, v6, v14
	v_pk_add_f16 v7, v7, v15
	v_pk_add_f16 v8, v8, v16
	v_pk_add_f16 v9, v9, v17
	v_pk_max_f16 v8, v8, 0
	v_pk_max_f16 v9, v9, 0
	v_pk_max_f16 v7, v7, 0
	v_pk_max_f16 v6, v6, 0
	v_pk_add_f16 v10, v10, v14
	v_pk_add_f16 v11, v11, v15
	v_pk_add_f16 v12, v12, v16
	v_pk_add_f16 v13, v13, v17
	v_pk_max_f16 v12, v12, 0
	v_pk_max_f16 v13, v13, 0
	v_pk_max_f16 v11, v11, 0
	v_pk_max_f16 v10, v10, 0
	ds_write_b128 v186, v[6:9] offset:16384
	ds_write_b128 v186, v[10:13] offset:24576
	s_nop 4
	global_load_dwordx4 v[6:9], v184, s[48:49]
	v_lshl_add_u64 v[18:19], s[34:35], 0, v[162:163]
	v_lshl_add_u64 v[22:23], s[26:27], 0, v[162:163]
	v_lshl_add_u64 v[24:25], s[26:27], 0, v[164:165]
	s_mov_b64 s[26:27], 0x80
	s_add_u32 s50, s30, 0x80
	global_load_dwordx4 v[10:13], v185, s[48:49]
	v_lshl_add_u64 v[20:21], s[34:35], 0, v[164:165]
	s_addc_u32 s51, s31, 0
	global_load_dwordx4 v[14:17], v183, s[50:51]
	s_add_i32 m0, s52, 0x18000
	v_lshl_add_u64 v[18:19], v[18:19], 0, s[26:27]
	global_load_lds_dwordx4 v[18:19], off
	v_lshl_add_u64 v[18:19], v[20:21], 0, s[26:27]
	s_add_i32 m0, s52, 0x1a000
	s_add_u32 s28, s28, 0x2080
	global_load_lds_dwordx4 v[18:19], off
	s_waitcnt vmcnt(2)
	s_addc_u32 s29, s29, 0
	v_pk_add_f16 v6, v6, v14
	v_pk_add_f16 v7, v7, v15
	v_pk_add_f16 v8, v8, v16
	v_pk_add_f16 v9, v9, v17
	v_pk_max_f16 v8, v8, 0
	v_pk_max_f16 v9, v9, 0
	v_pk_max_f16 v7, v7, 0
	v_pk_max_f16 v6, v6, 0
	v_pk_add_f16 v10, v10, v14
	v_pk_add_f16 v11, v11, v15
	v_pk_add_f16 v12, v12, v16
	v_pk_add_f16 v13, v13, v17
	v_pk_max_f16 v12, v12, 0
	v_pk_max_f16 v13, v13, 0
	v_pk_max_f16 v11, v11, 0
	v_pk_max_f16 v10, v10, 0
	ds_write_b128 v186, v[6:9] offset:32768
	ds_write_b128 v186, v[10:13] offset:40960
	s_nop 4
	global_load_dwordx4 v[14:17], v184, s[28:29]
	s_add_u32 s30, s30, 0x4080
	global_load_dwordx4 v[6:9], v185, s[28:29]
	s_addc_u32 s31, s31, 0
	global_load_dwordx4 v[10:13], v183, s[30:31]
	s_add_i32 m0, s52, 0x1c000
	v_lshl_add_u64 v[18:19], v[22:23], 0, s[26:27]
	global_load_lds_dwordx4 v[18:19], off
	v_lshl_add_u64 v[18:19], v[24:25], 0, s[26:27]
	s_add_i32 m0, s52, 0x1e000
	s_load_dword s29, s[0:1], 0x60
	global_load_lds_dwordx4 v[18:19], off
	s_cmp_lg_u32 s37, 1
	s_mov_b32 s48, 0
	s_cbranch_scc1 .LBB8_7
	s_barrier

.LBB8_11:
	s_add_u32 s59, s34, 0x100
	v_mov_b32_e32 v18, 0
	s_addc_u32 s60, s35, 0
	s_mov_b32 s61, 0
	s_movk_i32 s62, 0x80
	v_mov_b32_e32 v19, v18
	v_mov_b32_e32 v20, v18
	v_mov_b32_e32 v21, v18
	v_mov_b32_e32 v22, v18
	v_mov_b32_e32 v23, v18
	v_mov_b32_e32 v24, v18
	v_mov_b32_e32 v25, v18
	s_cmp_eq_u32 s83, 0
	s_mov_b32 s83, 1
	s_cbranch_scc1 .Lgu_skipzero
	v_mov_b64_e32 v[26:27], 0
	v_mov_b64_e32 v[28:29], 0
	v_mov_b64_e32 v[30:31], 0
	v_mov_b64_e32 v[32:33], 0
	v_mov_b64_e32 v[34:35], 0
	v_mov_b64_e32 v[36:37], 0
	v_mov_b64_e32 v[38:39], 0
	v_mov_b64_e32 v[40:41], 0
	v_mov_b64_e32 v[42:43], 0
	v_mov_b64_e32 v[44:45], 0
	v_mov_b64_e32 v[46:47], 0
	v_mov_b64_e32 v[48:49], 0
	v_mov_b64_e32 v[50:51], 0
	v_mov_b64_e32 v[52:53], 0
	v_mov_b64_e32 v[54:55], 0
	v_mov_b64_e32 v[56:57], 0
	v_mov_b64_e32 v[58:59], 0
	v_mov_b64_e32 v[60:61], 0
	v_mov_b64_e32 v[62:63], 0
	v_mov_b64_e32 v[64:65], 0
	v_mov_b64_e32 v[66:67], 0
	v_mov_b64_e32 v[68:69], 0
	v_mov_b64_e32 v[70:71], 0
	v_mov_b64_e32 v[72:73], 0
	v_mov_b64_e32 v[74:75], 0
	v_mov_b64_e32 v[76:77], 0
	v_mov_b64_e32 v[78:79], 0
	v_mov_b64_e32 v[80:81], 0
	v_mov_b64_e32 v[82:83], 0
	v_mov_b64_e32 v[84:85], 0
	v_mov_b64_e32 v[86:87], 0
	v_mov_b64_e32 v[88:89], 0
	v_mov_b64_e32 v[90:91], 0
	v_mov_b64_e32 v[92:93], 0
	v_mov_b64_e32 v[94:95], 0
	v_mov_b64_e32 v[96:97], 0
	v_mov_b64_e32 v[98:99], 0
	v_mov_b64_e32 v[100:101], 0
	v_mov_b64_e32 v[102:103], 0
	v_mov_b64_e32 v[104:105], 0
	v_mov_b64_e32 v[106:107], 0
	v_mov_b64_e32 v[108:109], 0
	v_mov_b64_e32 v[110:111], 0
	v_mov_b64_e32 v[112:113], 0
	v_mov_b64_e32 v[114:115], 0
	v_mov_b64_e32 v[116:117], 0
	v_mov_b64_e32 v[118:119], 0
	v_mov_b64_e32 v[120:121], 0
	v_mov_b64_e32 v[122:123], 0
	v_mov_b64_e32 v[124:125], 0
	v_mov_b64_e32 v[126:127], 0
	v_mov_b64_e32 v[128:129], 0
	v_mov_b64_e32 v[130:131], 0
	v_mov_b64_e32 v[132:133], 0
	v_mov_b64_e32 v[134:135], 0
	v_mov_b64_e32 v[136:137], 0
	v_mov_b64_e32 v[138:139], 0
	v_mov_b64_e32 v[140:141], 0
	v_mov_b64_e32 v[142:143], 0
	v_mov_b64_e32 v[144:145], 0

.Lgt_nobar:
	s_add_i32 m0, s34, 0x10000
	v_add_u32_e32 v175, 0, v1
	global_load_lds_dwordx4 v160, s[24:25]
	s_add_i32 m0, s34, 0x12000
	s_add_u32 s20, s4, 0x4000
	global_load_lds_dwordx4 v162, s[24:25]
	v_mov_b64_e32 v[24:25], 0
	v_mov_b64_e32 v[26:27], 0
	v_mov_b64_e32 v[28:29], 0
	v_mov_b64_e32 v[30:31], 0
	v_mov_b64_e32 v[32:33], 0
	v_mov_b64_e32 v[34:35], 0
	v_mov_b64_e32 v[36:37], 0
	v_mov_b64_e32 v[38:39], 0
	v_mov_b64_e32 v[40:41], 0
	v_mov_b64_e32 v[42:43], 0
	v_mov_b64_e32 v[44:45], 0
	v_mov_b64_e32 v[46:47], 0
	v_mov_b64_e32 v[48:49], 0
	v_mov_b64_e32 v[50:51], 0
	v_mov_b64_e32 v[52:53], 0
	v_mov_b64_e32 v[54:55], 0
	v_mov_b64_e32 v[56:57], 0
	v_mov_b64_e32 v[58:59], 0
	v_mov_b64_e32 v[60:61], 0
	v_mov_b64_e32 v[62:63], 0
	v_mov_b64_e32 v[64:65], 0
	v_mov_b64_e32 v[66:67], 0
	v_mov_b64_e32 v[68:69], 0
	v_mov_b64_e32 v[70:71], 0
	v_mov_b64_e32 v[72:73], 0
	v_mov_b64_e32 v[74:75], 0
	v_mov_b64_e32 v[76:77], 0
	v_mov_b64_e32 v[78:79], 0
	v_mov_b64_e32 v[80:81], 0
	v_mov_b64_e32 v[82:83], 0
	v_mov_b64_e32 v[84:85], 0
	v_mov_b64_e32 v[86:87], 0
	v_mov_b64_e32 v[88:89], 0
	v_mov_b64_e32 v[90:91], 0
	v_mov_b64_e32 v[92:93], 0
	v_mov_b64_e32 v[94:95], 0
	v_mov_b64_e32 v[96:97], 0
	v_mov_b64_e32 v[98:99], 0
	v_mov_b64_e32 v[100:101], 0
	v_mov_b64_e32 v[102:103], 0
	v_mov_b64_e32 v[104:105], 0
	v_mov_b64_e32 v[106:107], 0
	v_mov_b64_e32 v[108:109], 0
	v_mov_b64_e32 v[110:111], 0
	v_mov_b64_e32 v[112:113], 0
	v_mov_b64_e32 v[114:115], 0
	v_mov_b64_e32 v[116:117], 0
	v_mov_b64_e32 v[118:119], 0
	v_mov_b64_e32 v[120:121], 0
	v_mov_b64_e32 v[122:123], 0
	v_mov_b64_e32 v[124:125], 0
	v_mov_b64_e32 v[126:127], 0
	v_mov_b64_e32 v[128:129], 0
	v_mov_b64_e32 v[130:131], 0
	v_mov_b64_e32 v[132:133], 0
	v_mov_b64_e32 v[134:135], 0
	v_mov_b64_e32 v[136:137], 0
	v_mov_b64_e32 v[138:139], 0
	v_mov_b64_e32 v[140:141], 0
	v_mov_b64_e32 v[142:143], 0
	s_waitcnt vmcnt(2)
	s_addc_u32 s21, s5, 0
	v_pk_add_f16 v0, v2, v10
	v_pk_add_f16 v2, v3, v11
	v_pk_add_f16 v3, v4, v12
	v_pk_add_f16 v4, v5, v13
	s_add_u32 s28, s6, 0x8000
	v_pk_max_f16 v5, v4, 0
	v_pk_max_f16 v4, v3, 0
	v_pk_max_f16 v3, v2, 0
	v_pk_max_f16 v2, v0, 0
	v_pk_add_f16 v0, v6, v14
	v_pk_add_f16 v6, v7, v15
	v_pk_add_f16 v7, v8, v16
	v_pk_add_f16 v8, v9, v17
	s_addc_u32 s29, s7, 0
	v_pk_max_f16 v9, v8, 0
	v_pk_max_f16 v8, v7, 0
	v_pk_max_f16 v7, v6, 0
	v_pk_max_f16 v6, v0, 0
	ds_write_b128 v175, v[2:5]
	ds_write_b128 v175, v[6:9] offset:8192
	s_nop 4
	global_load_dwordx4 v[0:3], v168, s[20:21]
	global_load_dwordx4 v[4:7], v170, s[20:21]
	global_load_dwordx4 v[8:11], v169, s[28:29]
	s_add_u32 s20, s24, s14
	global_load_dwordx4 v[12:15], v171, s[28:29]
	s_addc_u32 s21, s25, s15
	s_add_i32 m0, s34, 0x14000
	v_mov_b32_e32 v161, 0
	global_load_lds_dwordx4 v160, s[20:21]
	s_add_i32 m0, s34, 0x16000
	s_add_u32 s28, s4, 0x80
	global_load_lds_dwordx4 v162, s[20:21]
	s_waitcnt vmcnt(2)
	s_addc_u32 s29, s5, 0
	v_pk_add_f16 v0, v0, v8
	v_pk_add_f16 v1, v1, v9
	v_pk_add_f16 v2, v2, v10
	v_pk_add_f16 v3, v3, v11
	v_pk_max_f16 v2, v2, 0
	v_pk_max_f16 v3, v3, 0
	v_pk_max_f16 v1, v1, 0
	v_pk_max_f16 v0, v0, 0
	v_pk_add_f16 v4, v4, v12
	v_pk_add_f16 v5, v5, v13
	v_pk_add_f16 v6, v6, v14
	v_pk_add_f16 v7, v7, v15
	v_pk_max_f16 v6, v6, 0
	v_pk_max_f16 v7, v7, 0
	v_pk_max_f16 v5, v5, 0
	v_pk_max_f16 v4, v4, 0
	ds_write_b128 v175, v[0:3] offset:16384
	ds_write_b128 v175, v[4:7] offset:24576
	s_nop 4
	global_load_dwordx4 v[0:3], v168, s[28:29]
	v_mov_b32_e32 v163, v161
	s_add_u32 s30, s6, 0x80
	global_load_dwordx4 v[4:7], v170, s[28:29]
	v_lshl_add_u64 v[18:19], s[24:25], 0, v[160:161]
	v_lshl_add_u64 v[16:17], s[20:21], 0, v[160:161]
	v_lshl_add_u64 v[22:23], s[20:21], 0, v[162:163]
	s_mov_b64 s[20:21], 0x80
	s_addc_u32 s31, s7, 0
	global_load_dwordx4 v[8:11], v169, s[30:31]
	v_lshl_add_u64 v[20:21], s[24:25], 0, v[162:163]
	global_load_dwordx4 v[12:15], v171, s[30:31]
	s_add_i32 m0, s34, 0x18000
	v_lshl_add_u64 v[18:19], v[18:19], 0, s[20:21]
	global_load_lds_dwordx4 v[18:19], off
	v_lshl_add_u64 v[18:19], v[20:21], 0, s[20:21]
	s_add_i32 m0, s34, 0x1a000
	s_add_u32 s4, s4, 0x4080
	global_load_lds_dwordx4 v[18:19], off
	s_waitcnt vmcnt(2)
	s_addc_u32 s5, s5, 0
	v_pk_add_f16 v0, v0, v8
	v_pk_add_f16 v1, v1, v9
	v_pk_add_f16 v2, v2, v10
	v_pk_add_f16 v3, v3, v11
	v_pk_max_f16 v2, v2, 0
	v_pk_max_f16 v3, v3, 0
	v_pk_max_f16 v1, v1, 0
	v_pk_max_f16 v0, v0, 0
	v_pk_add_f16 v4, v4, v12
	v_pk_add_f16 v5, v5, v13
	v_pk_add_f16 v6, v6, v14
	v_pk_add_f16 v7, v7, v15
	v_pk_max_f16 v6, v6, 0
	v_pk_max_f16 v7, v7, 0
	v_pk_max_f16 v5, v5, 0
	v_pk_max_f16 v4, v4, 0
	ds_write_b128 v175, v[0:3] offset:32768
	ds_write_b128 v175, v[4:7] offset:40960
	s_nop 4
	global_load_dwordx4 v[8:11], v168, s[4:5]
	s_add_u32 s6, s6, 0x8080
	global_load_dwordx4 v[0:3], v170, s[4:5]
	s_addc_u32 s7, s7, 0
	global_load_dwordx4 v[12:15], v169, s[6:7]
	global_load_dwordx4 v[4:7], v171, s[6:7]
	s_add_i32 m0, s34, 0x1c000
	v_lshl_add_u64 v[16:17], v[16:17], 0, s[20:21]
	global_load_lds_dwordx4 v[16:17], off
	v_lshl_add_u64 v[16:17], v[22:23], 0, s[20:21]
	s_add_i32 m0, s34, 0x1e000
	s_cmp_lg_u32 s27, 1
	global_load_lds_dwordx4 v[16:17], off
	s_load_dwordx4 s[4:7], s[0:1], 0x68
	s_load_dword s47, s[0:1], 0x78
	s_mov_b32 s48, 0
	s_cbranch_scc1 .LBB8_32
	s_barrier
